# MoE GEMM phases reuse the expert tile-offset table the permute phase left in LDS instead of reloading the counters
# speedup vs baseline: 1.0029x; 1.0029x over previous
.LBB0_986:
	v_readlane_b32 s0, v254, 27
	v_readlane_b32 s1, v254, 28
	s_andn2_b64 vcc, exec, s[0:1]
	s_cbranch_vccnz .LBB0_1177
	s_mov_b64 s[4:5], s[88:89]
	s_load_dwordx2 s[0:1], s[4:5], 0x98
	s_mov_b64 s[6:7], exec
	v_readlane_b32 s8, v253, 4
	v_readlane_b32 s9, v253, 5
	s_and_b64 s[8:9], s[6:7], s[8:9]
	s_mov_b64 exec, s[8:9]
	s_branch .LBB0_989

.LBB0_1177:
	v_readlane_b32 s0, v254, 32
	v_readlane_b32 s1, v254, 33
	s_andn2_b64 vcc, exec, s[0:1]
	s_cbranch_vccnz .LBB0_1366
	s_mov_b64 s[6:7], s[88:89]
	s_load_dwordx2 s[28:29], s[6:7], 0x98
	s_mov_b64 s[0:1], exec
	v_readlane_b32 s4, v253, 4
	v_readlane_b32 s5, v253, 5
	s_and_b64 s[4:5], s[0:1], s[4:5]
	s_mov_b64 exec, s[4:5]
	s_branch .LBB0_1180
